# 2-CU split + half-batch LDS fragment reads with counted waits + peerdown wait fix
# speedup vs baseline: 1.0125x; 1.0125x over previous
; DI void gdn_scan_seq(const Params& p, int bh16, char* ldsf) {
;     ...
;   f32x16 S[4];
; #pragma unroll
;   for (int m = 0; m < 4; ++m)
; #pragma unroll
;     for (int r = 0; r < 16; ++r) S[m][r] = 0.f;
;   asm volatile("s_waitcnt vmcnt(0)" ::: "memory");
;   __syncthreads();
;   SCAN_ISSUE(0, 0); SCAN_ISSUE(1, 1);
; DI void phase_mixer(const Params& p, int bid, int nb, char* lds, char* ctl, char* ldsf) {
;     ...
;   if (bid < 32) { if (vb == 0) gdn_scan_seq(p, bid >> 1, ldsf); else { __syncthreads(); for (int k = 0; k < 128; ++k) { __builtin_amdgcn_s_barrier(); asm volatile("" ::: "memory"); } __syncthreads(); } }
.LBB0_1207:
	s_or_b64 exec, exec, s[0:1]
	v_mov_b32_e32 v135, v206
	s_waitcnt lgkmcnt(0)
	s_barrier
	s_movk_i32 s2, 64
	v_cmp_gt_i32_e64 s[6:7], s2, v176
	s_nop 3
	s_and_saveexec_b64 s[0:1], s[6:7]
	s_cbranch_execz .LBB0_1227
	s_movk_i32 s2, 0xff
	v_cmp_lt_u32_e32 vcc, s2, v207
	s_and_saveexec_b64 s[2:3], vcc
	s_xor_b64 s[6:7], exec, s[2:3]
	s_cbranch_execz .LBB0_1212
	v_readlane_b32 s2, v250, 0
	v_lshrrev_b32_e32 v209, 6, v206
	v_and_b32_e32 v208, 63, v206
	v_lshlrev_b32_e32 v132, 12, v209
	v_lshl_or_b32 v132, v208, 4, v132
	v_readfirstlane_b32 s3, v209
	s_nop 3
	s_lshr_b32 s18, s2, 4
	s_and_b32 s2, s2, 15
	s_cmp_lt_u32 s3, 2
	s_cselect_b64 s[16:17], -1, 0
	v_and_b32_e32 v209, 1, v209
	v_lshl_add_u32 v209, s18, 1, v209
	v_lshlrev_b32_e32 v133, 11, v209
	v_lshl_or_b32 v133, v208, 5, v133
	v_add_u32_e32 v134, 0x2000, v133
	v_lshlrev_b32_e32 v210, 12, v209
	v_lshl_or_b32 v210, v208, 4, v210
	v_mov_b32_e32 v208, v132
	s_lshl_b32 s2, s2, 21
	s_add_u32 s8, s84, s2
	s_addc_u32 s9, s85, 0
	s_add_u32 s12, s8, 0x1c000000
	s_addc_u32 s13, s9, 0
	s_add_u32 s8, s8, 0x1e000000
	s_addc_u32 s9, s9, 0
	s_add_u32 s10, s66, s2
	s_addc_u32 s11, s67, 0
	s_add_u32 s10, s10, 0x2000000
	s_addc_u32 s11, s11, 0
	s_mov_b32 s15, 0
	global_load_dwordx4 v[0:3], v132, s[8:9]
	global_load_dwordx4 v[4:7], v132, s[8:9] offset:1024
	global_load_dwordx4 v[8:11], v132, s[8:9] offset:2048
	global_load_dwordx4 v[12:15], v132, s[8:9] offset:3072
	global_load_dwordx4 v[16:19], v132, s[10:11]
	global_load_dwordx4 v[20:23], v132, s[10:11] offset:1024
	global_load_dwordx4 v[24:27], v132, s[10:11] offset:2048
	global_load_dwordx4 v[28:31], v132, s[10:11] offset:3072
	global_load_dwordx4 v[32:35], v133, s[12:13]
	global_load_dwordx4 v[36:39], v133, s[12:13] offset:16
	global_load_dwordx4 v[40:43], v134, s[12:13]
	global_load_dwordx4 v[44:47], v134, s[12:13] offset:16
	s_add_u32 s15, s15, 1
	s_cmp_lt_u32 s15, 0x80
	s_cselect_b32 s14, 0x4000, 0
	s_add_u32 s8, s8, s14
	s_addc_u32 s9, s9, 0
	s_add_u32 s10, s10, s14
	s_addc_u32 s11, s11, 0
	s_add_u32 s12, s12, s14
	s_addc_u32 s13, s13, 0
	global_load_dwordx4 v[48:51], v132, s[8:9]
	global_load_dwordx4 v[52:55], v132, s[8:9] offset:1024
	global_load_dwordx4 v[56:59], v132, s[8:9] offset:2048
	global_load_dwordx4 v[60:63], v132, s[8:9] offset:3072
	global_load_dwordx4 v[64:67], v132, s[10:11]
	global_load_dwordx4 v[68:71], v132, s[10:11] offset:1024
	global_load_dwordx4 v[72:75], v132, s[10:11] offset:2048
	global_load_dwordx4 v[76:79], v132, s[10:11] offset:3072
	global_load_dwordx4 v[80:83], v133, s[12:13]
	global_load_dwordx4 v[84:87], v133, s[12:13] offset:16
	global_load_dwordx4 v[88:91], v134, s[12:13]
	global_load_dwordx4 v[92:95], v134, s[12:13] offset:16
	s_add_u32 s15, s15, 1
	s_cmp_lt_u32 s15, 0x80
	s_cselect_b32 s14, 0x4000, 0
	s_add_u32 s8, s8, s14
	s_addc_u32 s9, s9, 0
	s_add_u32 s10, s10, s14
	s_addc_u32 s11, s11, 0
	s_add_u32 s12, s12, s14
	s_addc_u32 s13, s13, 0
	global_load_dwordx4 v[96:99], v132, s[8:9]
	global_load_dwordx4 v[100:103], v132, s[8:9] offset:1024
	global_load_dwordx4 v[104:107], v132, s[8:9] offset:2048
	global_load_dwordx4 v[108:111], v132, s[8:9] offset:3072
	global_load_dwordx4 v[112:115], v132, s[10:11]
	global_load_dwordx4 v[116:119], v132, s[10:11] offset:1024
	global_load_dwordx4 v[120:123], v132, s[10:11] offset:2048
	global_load_dwordx4 v[124:127], v132, s[10:11] offset:3072
	global_load_dwordx4 v[128:131], v133, s[12:13]
	global_load_dwordx4 v[136:139], v133, s[12:13] offset:16
	global_load_dwordx4 v[140:143], v134, s[12:13]
	global_load_dwordx4 v[148:151], v134, s[12:13] offset:16
	s_add_u32 s15, s15, 1
	s_cmp_lt_u32 s15, 0x80
	s_cselect_b32 s14, 0x4000, 0
	s_add_u32 s8, s8, s14
	s_addc_u32 s9, s9, 0
	s_add_u32 s10, s10, s14
	s_addc_u32 s11, s11, 0
	s_add_u32 s12, s12, s14
	s_addc_u32 s13, s13, 0
	global_load_dwordx4 v[152:155], v132, s[8:9]
	global_load_dwordx4 v[156:159], v132, s[8:9] offset:1024
	global_load_dwordx4 v[160:163], v132, s[8:9] offset:2048
	global_load_dwordx4 v[164:167], v132, s[8:9] offset:3072
	global_load_dwordx4 v[168:171], v132, s[10:11]
	global_load_dwordx4 v[172:175], v132, s[10:11] offset:1024
	global_load_dwordx4 v[178:181], v132, s[10:11] offset:2048
	global_load_dwordx4 v[182:185], v132, s[10:11] offset:3072
	global_load_dwordx4 v[190:193], v133, s[12:13]
	global_load_dwordx4 v[194:197], v133, s[12:13] offset:16
	global_load_dwordx4 v[198:201], v134, s[12:13]
	global_load_dwordx4 v[202:205], v134, s[12:13] offset:16
	s_add_u32 s15, s15, 1
	s_cmp_lt_u32 s15, 0x80
	s_cselect_b32 s14, 0x4000, 0
	s_add_u32 s8, s8, s14
	s_addc_u32 s9, s9, 0
	s_add_u32 s10, s10, s14
	s_addc_u32 s11, s11, 0
	s_add_u32 s12, s12, s14
	s_addc_u32 s13, s13, 0
	s_mov_b32 s2, 0
	s_mov_b32 s3, 0
	s_barrier

; DI float bflo(unsigned u) { return __uint_as_float(u << 16); }
; DI float bfhi(unsigned u) { return __uint_as_float(u & 0xffff0000u); }
; #define SCAN_RDW(F, mh) do { _Pragma("unroll") for (int k = 0; k < 8; ++k) { const int i2 = k >> 2, m = 2 * (mh) + ((k >> 1) & 1), sx = k & 1; F[k] = *(const bf16x8*)(lw + ((i2 * 4 + m) * 2 + sx) * 1024); } } while (0)
; #define SCAN_RDK(F, mh) do { _Pragma("unroll") for (int k = 0; k < 8; ++k) { const int m = 2 * (mh) + (k >> 2), j2 = (k >> 1) & 1, sx = k & 1; F[k] = *(const bf16x8*)(lk + ((m * 2 + j2) * 2 + sx) * 1024); } } while (0)
; #define SCAN_MMW(F, mh) do { _Pragma("unroll") for (int q = 0; q < 4; ++q) { const int m = 2 * (mh) + (q >> 1), sx = q & 1; vn[0] = MFMA32(F[q], Sb[m][sx], vn[0]); vn[1] = MFMA32(F[4 + q], Sb[m][sx], vn[1]); } } while (0)
; DI void gdn_scan_seq(const Params& p, int bh16, char* ldsf) {
;     ...
;     const char* lw = base + lane * 16; const char* lk = lw + 16384; const char* lu = base + 32768 + wv * 4096 + lane * 16;
;     const float gl = glt[c];
;     f32x16 vn[2];
; #pragma unroll
;     for (int i2 = 0; i2 < 2; ++i2) {
;       const u32x4 ua = *(const u32x4*)(lu + (2 * i2) * 1024), ub = *(const u32x4*)(lu + (2 * i2 + 1) * 1024);
; #pragma unroll
;       for (int e = 0; e < 4; ++e) { vn[i2][2 * e] = bflo(ua[e]); vn[i2][2 * e + 1] = bfhi(ua[e]); vn[i2][8 + 2 * e] = bflo(ub[e]); vn[i2][8 + 2 * e + 1] = bfhi(ub[e]); }
;     }
;     bf16x8 fa[8], fb[8];
;     ...
;     SCAN_RDW(fa, 0);
;     __builtin_amdgcn_sched_barrier(0);
;     SCAN_RDW(fb, 1);
;     __builtin_amdgcn_sched_barrier(0);
;     SCAN_MMW(fa, 0);
;     __builtin_amdgcn_sched_barrier(0);
;     SCAN_RDK(fa, 0);
;     __builtin_amdgcn_sched_barrier(0);
;     SCAN_MMW(fb, 1);
;     __builtin_amdgcn_sched_barrier(0);
;     SCAN_RDK(fb, 1);
;     __builtin_amdgcn_sched_barrier(0);
.Lscan_noprog:
	v_add_u32_e32 v131, s3, v130
	v_add_u32_e32 v134, s3, v129
	v_mov_b32_e32 v143, s18
	ds_read_b128 v[72:75], v134 offset:32768
	ds_read_b128 v[76:79], v134 offset:33792
	ds_read_b32 v142, v143
	ds_read_b128 v[148:151], v131 offset:0
	ds_read_b128 v[152:155], v131 offset:1024
	ds_read_b128 v[156:159], v131 offset:2048
	ds_read_b128 v[160:163], v131 offset:3072
	ds_read_b128 v[164:167], v131 offset:4096
	ds_read_b128 v[168:171], v131 offset:5120
	ds_read_b128 v[172:175], v131 offset:6144
	ds_read_b128 v[178:181], v131 offset:7168
	ds_read_b128 v[88:91], v134 offset:34816
	ds_read_b128 v[92:95], v134 offset:35840
	s_waitcnt lgkmcnt(10)
	v_mfma_f32_32x32x16_bf16 v[0:15], v[182:185], v[80:83], v[0:15]
	v_lshlrev_b32_e32 v64, 16, v72
	v_and_b32_e32 v65, 0xffff0000, v72
	v_lshlrev_b32_e32 v66, 16, v73
	v_and_b32_e32 v67, 0xffff0000, v73
	v_mfma_f32_32x32x16_bf16 v[0:15], v[190:193], v[84:87], v[0:15]
	v_lshlrev_b32_e32 v68, 16, v74
	v_and_b32_e32 v69, 0xffff0000, v74
	v_lshlrev_b32_e32 v70, 16, v75
	v_and_b32_e32 v71, 0xffff0000, v75
	v_mfma_f32_32x32x16_bf16 v[16:31], v[194:197], v[80:83], v[16:31]
	v_lshlrev_b32_e32 v72, 16, v76
	v_and_b32_e32 v73, 0xffff0000, v76
	v_lshlrev_b32_e32 v74, 16, v77
	v_and_b32_e32 v75, 0xffff0000, v77
	v_mfma_f32_32x32x16_bf16 v[16:31], v[198:201], v[84:87], v[16:31]
	v_lshlrev_b32_e32 v76, 16, v78
	v_and_b32_e32 v77, 0xffff0000, v78
	v_lshlrev_b32_e32 v78, 16, v79
	v_and_b32_e32 v79, 0xffff0000, v79
	s_waitcnt lgkmcnt(8)
	ds_read_b128 v[182:185], v131 offset:8192
	ds_read_b128 v[190:193], v131 offset:9216
	ds_read_b128 v[194:197], v131 offset:10240
	ds_read_b128 v[198:201], v131 offset:11264
	v_mfma_f32_32x32x16_bf16 v[32:47], v[202:205], v[80:83], v[32:47]
	v_cvt_pk_bf16_f32 v96, v0, v1
	v_cvt_pk_bf16_f32 v97, v2, v3
	v_cvt_pk_bf16_f32 v98, v4, v5
	v_cvt_pk_bf16_f32 v99, v6, v7
	v_cvt_pk_bf16_f32 v100, v8, v9
	v_mfma_f32_32x32x16_bf16 v[32:47], v[208:211], v[84:87], v[32:47]
	v_cvt_pk_bf16_f32 v101, v10, v11
	v_cvt_pk_bf16_f32 v102, v12, v13
	v_cvt_pk_bf16_f32 v103, v14, v15
	v_mfma_f32_32x32x16_bf16 v[48:63], v[212:215], v[80:83], v[48:63]
	v_cvt_pk_bf16_f32 v104, v16, v17
	v_cvt_pk_bf16_f32 v105, v18, v19
	v_cvt_pk_bf16_f32 v106, v20, v21
	v_cvt_pk_bf16_f32 v107, v22, v23
	v_cvt_pk_bf16_f32 v108, v24, v25
	v_mfma_f32_32x32x16_bf16 v[48:63], v[216:219], v[84:87], v[48:63]
	v_cvt_pk_bf16_f32 v109, v26, v27
	v_cvt_pk_bf16_f32 v110, v28, v29
	v_cvt_pk_bf16_f32 v111, v30, v31
	s_waitcnt lgkmcnt(4)
	ds_read_b128 v[202:205], v131 offset:12288
	ds_read_b128 v[208:211], v131 offset:13312
	ds_read_b128 v[212:215], v131 offset:14336
	ds_read_b128 v[216:219], v131 offset:15360
	v_mfma_f32_32x32x16_bf16 v[64:79], v[148:151], v[96:99], v[64:79]
	v_cvt_pk_bf16_f32 v112, v32, v33
	v_cvt_pk_bf16_f32 v113, v34, v35
	v_cvt_pk_bf16_f32 v114, v36, v37
	v_cvt_pk_bf16_f32 v115, v38, v39
	v_lshlrev_b32_e32 v80, 16, v88
	v_mfma_f32_32x32x16_bf16 v[64:79], v[152:155], v[100:103], v[64:79]
	v_cvt_pk_bf16_f32 v116, v40, v41
	v_cvt_pk_bf16_f32 v117, v42, v43
	v_cvt_pk_bf16_f32 v118, v44, v45
	v_cvt_pk_bf16_f32 v119, v46, v47
	v_and_b32_e32 v81, 0xffff0000, v88
	v_mfma_f32_32x32x16_bf16 v[64:79], v[156:159], v[104:107], v[64:79]
	v_cvt_pk_bf16_f32 v120, v48, v49
	v_cvt_pk_bf16_f32 v121, v50, v51
	v_cvt_pk_bf16_f32 v122, v52, v53
	v_cvt_pk_bf16_f32 v123, v54, v55
	v_lshlrev_b32_e32 v82, 16, v89
	v_mfma_f32_32x32x16_bf16 v[64:79], v[160:163], v[108:111], v[64:79]
	v_cvt_pk_bf16_f32 v124, v56, v57
	v_cvt_pk_bf16_f32 v125, v58, v59
	v_cvt_pk_bf16_f32 v126, v60, v61
	v_cvt_pk_bf16_f32 v127, v62, v63
	v_and_b32_e32 v83, 0xffff0000, v89
	ds_read_b128 v[148:151], v131 offset:16384
	ds_read_b128 v[152:155], v131 offset:17408
	ds_read_b128 v[156:159], v131 offset:20480
	ds_read_b128 v[160:163], v131 offset:21504
	v_mfma_f32_32x32x16_bf16 v[64:79], v[164:167], v[112:115], v[64:79]
	v_lshlrev_b32_e32 v84, 16, v90
	v_and_b32_e32 v85, 0xffff0000, v90
	v_lshlrev_b32_e32 v86, 16, v91
	v_and_b32_e32 v87, 0xffff0000, v91
	v_lshlrev_b32_e32 v88, 16, v92
	global_store_dwordx4 v128, v[96:99], s[8:9]
	v_mfma_f32_32x32x16_bf16 v[64:79], v[168:171], v[116:119], v[64:79]
	v_and_b32_e32 v89, 0xffff0000, v92
	v_lshlrev_b32_e32 v90, 16, v93
	v_and_b32_e32 v91, 0xffff0000, v93
	v_lshlrev_b32_e32 v92, 16, v94
	v_and_b32_e32 v93, 0xffff0000, v94
	global_store_dwordx4 v128, v[100:103], s[8:9] offset:1024
	v_mfma_f32_32x32x16_bf16 v[64:79], v[172:175], v[120:123], v[64:79]
	v_lshlrev_b32_e32 v94, 16, v95
	v_and_b32_e32 v95, 0xffff0000, v95
	global_store_dwordx4 v128, v[104:107], s[8:9] offset:2048
	global_store_dwordx4 v128, v[108:111], s[8:9] offset:3072
	v_mul_f32_e32 v0, v142, v0
	v_mfma_f32_32x32x16_bf16 v[64:79], v[178:181], v[124:127], v[64:79]
	v_mul_f32_e32 v1, v142, v1
	v_mul_f32_e32 v2, v142, v2
	v_mul_f32_e32 v3, v142, v3
	v_mul_f32_e32 v4, v142, v4
	v_mul_f32_e32 v5, v142, v5
	s_waitcnt lgkmcnt(8)
; DI bf16x8 packS(const f32x16& x, int s) { return pack8(x[8 * s], x[8 * s + 1], x[8 * s + 2], x[8 * s + 3], x[8 * s + 4], x[8 * s + 5], x[8 * s + 6], x[8 * s + 7]); }
; #define SCAN_RDK(F, mh) do { _Pragma("unroll") for (int k = 0; k < 8; ++k) { const int m = 2 * (mh) + (k >> 2), j2 = (k >> 1) & 1, sx = k & 1; F[k] = *(const bf16x8*)(lk + ((m * 2 + j2) * 2 + sx) * 1024); } } while (0)
; #define SCAN_MMK(F, mh) do { _Pragma("unroll") for (int q = 0; q < 4; ++q) { const int j2 = q >> 1, sx = q & 1; S[2 * (mh)] = MFMA32(F[q], Vb[j2][sx], S[2 * (mh)]); S[2 * (mh) + 1] = MFMA32(F[4 + q], Vb[j2][sx], S[2 * (mh) + 1]); } } while (0)
; DI void gdn_scan_seq(const Params& p, int bh16, char* ldsf) {
;     ...
;     SCAN_RDK(fb, 1);
;     __builtin_amdgcn_sched_barrier(0);
;     bf16x8 Vb[2][2];
; #pragma unroll
;     for (int j2 = 0; j2 < 2; ++j2) { Vb[j2][0] = packS(vn[j2], 0); Vb[j2][1] = packS(vn[j2], 1); }
; #pragma unroll
;     for (int m = 0; m < 4; ++m)
; #pragma unroll
;       for (int r = 0; r < 16; ++r) S[m][r] *= gl;
;     SCAN_MMK(fa, 0);
;     SCAN_MMK(fb, 1);
;     ...
;     asm volatile("s_waitcnt lgkmcnt(0)" ::: "memory");
;     sl = sl == 2 ? 0 : sl + 1;
;   }
	ds_read_b128 v[164:167], v131 offset:24576
	ds_read_b128 v[168:171], v131 offset:25600
	ds_read_b128 v[172:175], v131 offset:28672
	ds_read_b128 v[178:181], v131 offset:29696
	v_mfma_f32_32x32x16_bf16 v[80:95], v[182:185], v[96:99], v[80:95]
	v_mul_f32_e32 v6, v142, v6
	v_mul_f32_e32 v7, v142, v7
	v_mul_f32_e32 v8, v142, v8
	v_mul_f32_e32 v9, v142, v9
	v_mul_f32_e32 v10, v142, v10
	v_mfma_f32_32x32x16_bf16 v[80:95], v[190:193], v[100:103], v[80:95]
	v_mul_f32_e32 v11, v142, v11
	v_mul_f32_e32 v12, v142, v12
	v_mul_f32_e32 v13, v142, v13
	v_mul_f32_e32 v14, v142, v14
	v_mul_f32_e32 v15, v142, v15
	v_mfma_f32_32x32x16_bf16 v[80:95], v[194:197], v[104:107], v[80:95]
	v_mul_f32_e32 v16, v142, v16
	v_mul_f32_e32 v17, v142, v17
	v_mul_f32_e32 v18, v142, v18
	v_mul_f32_e32 v19, v142, v19
	global_store_dwordx4 v128, v[112:115], s[10:11]
	v_mul_f32_e32 v32, v142, v32
	v_mfma_f32_32x32x16_bf16 v[80:95], v[198:201], v[108:111], v[80:95]
	v_mul_f32_e32 v20, v142, v20
	v_mul_f32_e32 v21, v142, v21
	v_mul_f32_e32 v22, v142, v22
	v_mul_f32_e32 v23, v142, v23
	global_store_dwordx4 v128, v[116:119], s[10:11] offset:1024
	v_mul_f32_e32 v33, v142, v33
	s_waitcnt lgkmcnt(8)
	ds_read_b128 v[182:185], v131 offset:18432
	ds_read_b128 v[190:193], v131 offset:19456
	ds_read_b128 v[194:197], v131 offset:22528
	ds_read_b128 v[198:201], v131 offset:23552
	v_mfma_f32_32x32x16_bf16 v[80:95], v[202:205], v[112:115], v[80:95]
	v_mul_f32_e32 v24, v142, v24
	v_mul_f32_e32 v25, v142, v25
	v_mul_f32_e32 v26, v142, v26
	v_mul_f32_e32 v27, v142, v27
	global_store_dwordx4 v128, v[120:123], s[10:11] offset:2048
	v_mul_f32_e32 v34, v142, v34
	v_mfma_f32_32x32x16_bf16 v[80:95], v[208:211], v[116:119], v[80:95]
	v_mul_f32_e32 v28, v142, v28
	v_mul_f32_e32 v29, v142, v29
	v_mul_f32_e32 v30, v142, v30
	v_mul_f32_e32 v31, v142, v31
	global_store_dwordx4 v128, v[124:127], s[10:11] offset:3072
	v_mul_f32_e32 v35, v142, v35
	v_mfma_f32_32x32x16_bf16 v[80:95], v[212:215], v[120:123], v[80:95]
	v_cvt_pk_bf16_f32 v64, v64, v65
	v_cvt_pk_bf16_f32 v65, v66, v67
	v_cvt_pk_bf16_f32 v66, v68, v69
	v_cvt_pk_bf16_f32 v67, v70, v71
	v_cvt_pk_bf16_f32 v68, v72, v73
	v_mul_f32_e32 v36, v142, v36
	v_mfma_f32_32x32x16_bf16 v[80:95], v[216:219], v[124:127], v[80:95]
	v_cvt_pk_bf16_f32 v69, v74, v75
	v_cvt_pk_bf16_f32 v70, v76, v77
	v_cvt_pk_bf16_f32 v71, v78, v79
	v_mul_f32_e32 v37, v142, v37
	v_mul_f32_e32 v38, v142, v38
	v_mul_f32_e32 v39, v142, v39
	s_waitcnt lgkmcnt(8)
	ds_read_b128 v[202:205], v131 offset:26624
	ds_read_b128 v[208:211], v131 offset:27648
	ds_read_b128 v[212:215], v131 offset:30720
	ds_read_b128 v[216:219], v131 offset:31744
	v_mfma_f32_32x32x16_bf16 v[0:15], v[148:151], v[64:67], v[0:15]
	v_mul_f32_e32 v40, v142, v40
	v_mul_f32_e32 v41, v142, v41
	v_mul_f32_e32 v42, v142, v42
	v_mul_f32_e32 v43, v142, v43
	v_mul_f32_e32 v44, v142, v44
	v_mul_f32_e32 v45, v142, v45
	s_add_u32 s2, s2, 1
	s_xor_b32 s3, s3, 0xc000
	s_add_u32 s18, s18, 4
	s_add_u32 s8, s8, 0x8000
	s_addc_u32 s9, s9, 0
	s_add_u32 s10, s10, 0x8000
	s_addc_u32 s11, s11, 0
	v_mfma_f32_32x32x16_bf16 v[0:15], v[152:155], v[68:71], v[0:15]
	v_mul_f32_e32 v46, v142, v46
	v_mul_f32_e32 v47, v142, v47
	v_mul_f32_e32 v48, v142, v48
	v_mul_f32_e32 v49, v142, v49
	v_mul_f32_e32 v50, v142, v50
	v_mul_f32_e32 v51, v142, v51
	v_mfma_f32_32x32x16_bf16 v[16:31], v[156:159], v[64:67], v[16:31]
	v_mul_f32_e32 v52, v142, v52
	v_mul_f32_e32 v53, v142, v53
	v_mul_f32_e32 v54, v142, v54
	v_mul_f32_e32 v55, v142, v55
	v_mul_f32_e32 v56, v142, v56
	v_mul_f32_e32 v57, v142, v57
	v_mfma_f32_32x32x16_bf16 v[16:31], v[160:163], v[68:71], v[16:31]
	v_mul_f32_e32 v58, v142, v58
	v_mul_f32_e32 v59, v142, v59
	v_mul_f32_e32 v60, v142, v60
	v_mul_f32_e32 v61, v142, v61
	v_mul_f32_e32 v62, v142, v62
	v_mul_f32_e32 v63, v142, v63
	s_waitcnt lgkmcnt(8)
	v_mfma_f32_32x32x16_bf16 v[32:47], v[164:167], v[64:67], v[32:47]
	v_cvt_pk_bf16_f32 v80, v80, v81
	v_cvt_pk_bf16_f32 v81, v82, v83
	v_cvt_pk_bf16_f32 v82, v84, v85
	v_cvt_pk_bf16_f32 v83, v86, v87
	v_cvt_pk_bf16_f32 v84, v88, v89
	v_cvt_pk_bf16_f32 v85, v90, v91
	v_mfma_f32_32x32x16_bf16 v[32:47], v[168:171], v[68:71], v[32:47]
	v_cvt_pk_bf16_f32 v86, v92, v93
	v_cvt_pk_bf16_f32 v87, v94, v95
	v_mfma_f32_32x32x16_bf16 v[48:63], v[172:175], v[64:67], v[48:63]
	v_mfma_f32_32x32x16_bf16 v[48:63], v[178:181], v[68:71], v[48:63]
	s_cmp_lt_u32 s2, 0x80
	s_waitcnt lgkmcnt(0)
	s_cbranch_scc1 .Lscan_loop
	s_branch .Lscan_end
